# up-proj produces the quad's second row tile first (tile index xor 0x400) so the down-proj consumes the most recently written H first (cache-recency order)
# speedup vs baseline: 1.0073x; 1.0058x over previous
;     __host__ __device__ bool next(int i, Unit& u) const {
;         const long L = (long)i * G + c; if (L >= nwg) return false;
;         int wgid = (int)L; { const int q = nwg / NXCD, r = nwg % NXCD, xcd = wgid % NXCD, off = wgid / NXCD; wgid = (xcd < r ? xcd * (q + 1) : r * (q + 1) + (xcd - r) * q) + off; }
;         const int nig = WGM * nN, gid = wgid / nig, fm = gid * WGM, gsz = (nM - fm) < WGM ? (nM - fm) : WGM;
;         u.pm = fm + ((wgid % nig) % gsz); u.pn = (wgid % nig) / gsz; return true;
; template <class Epi, class Sched, bool ALIGN_EPI = false, bool SP2 = false>
; __device__ __forceinline__ void gemm_phase(PG8_LAS unsigned char* lds, const Gemm g, const Sched& S, const Epi& E, const int tid) {
;     ...
;     if (!S.next(0, cur)) return;
.LBB0_44:
	s_or_b64 exec, exec, s[8:9]
	s_andn2_b64 vcc, exec, s[6:7]
	v_readfirstlane_b32 s8, v232
	s_waitcnt lgkmcnt(0)
	s_barrier
	s_cbranch_vccnz .LBB0_68
	v_readlane_b32 s6, v254, 15
	s_xor_b32 s6, s6, 0x400
	s_lshr_b32 s0, s30, 29
	v_readlane_b32 s7, v254, 16
	s_add_i32 s7, s6, s0
	s_and_b32 s0, s7, -8
	s_sub_i32 s9, s6, s0
	s_cmp_gt_i32 s9, -1
	s_mov_b64 s[0:1], -1
	s_cbranch_scc0 .LBB0_47
	s_lshl_b32 s6, s9, 8
	s_mov_b64 s[0:1], 0

;     __host__ __device__ bool next(int i, Unit& u) const {
;         const long L = (long)i * G + c; if (L >= nwg) return false;
;         int wgid = (int)L; { const int q = nwg / NXCD, r = nwg % NXCD, xcd = wgid % NXCD, off = wgid / NXCD; wgid = (xcd < r ? xcd * (q + 1) : r * (q + 1) + (xcd - r) * q) + off; }
;         const int nig = WGM * nN, gid = wgid / nig, fm = gid * WGM, gsz = (nM - fm) < WGM ? (nM - fm) : WGM;
;         u.pm = fm + ((wgid % nig) % gsz); u.pn = (wgid % nig) / gsz; return true;
; template <class Epi, class Sched, bool ALIGN_EPI = false, bool SP2 = false>
; __device__ __forceinline__ void gemm_phase(PG8_LAS unsigned char* lds, const Gemm g, const Sched& S, const Epi& E, const int tid) {
;     ...
;         const bool has_next = S.next(ui + 1, nxt);
.LBB0_54:
	s_add_i32 s48, s48, 1
	v_readlane_b32 s3, v254, 12
	s_mul_i32 s0, s48, s31
	s_mul_hi_u32 s1, s48, s3
	s_add_i32 s1, s1, s0
	s_mul_i32 s0, s48, s3
	v_readlane_b32 s16, v254, 15
	v_readlane_b32 s17, v254, 16
	s_add_u32 s16, s0, s16
	s_addc_u32 s17, s1, s30
	v_mov_b64_e32 v[2:3], 0x800
	v_cmp_lt_i64_e64 s[0:1], s[16:17], v[2:3]
	v_mov_b64_e32 v[2:3], 0x7ff
	v_cmp_gt_i64_e32 vcc, s[16:17], v[2:3]
	s_cbranch_vccnz .LBB0_60
	s_xor_b32 s16, s16, 0x400
	s_ashr_i32 s12, s16, 31
	s_lshr_b32 s12, s12, 29
	s_add_i32 s14, s16, s12
	s_and_b32 s12, s14, -8
	s_sub_i32 s15, s16, s12
	s_cmp_gt_i32 s15, -1
	s_mov_b64 s[12:13], -1
	s_cbranch_scc0 .LBB0_57
	s_lshl_b32 s16, s15, 8
	s_mov_b64 s[12:13], 0
